# attention static priority raise given to waves 0-3 instead of 4-7 (per-half comparison)
# baseline (speedup 1.0000x reference)
.LBB0_1190:
	v_readlane_b32 s10, v254, 0
	s_cmp_le_i32 s10, s0
	s_cselect_b64 s[0:1], -1, 0
	s_and_b64 s[18:19], s[0:1], s[26:27]
	s_andn2_b64 vcc, exec, s[18:19]
	v_readlane_b32 s11, v254, 1
	s_cbranch_vccnz .LBB0_1368
	s_mov_b32 s100, m0
	v_readlane_b32 s12, v254, 2
	v_readlane_b32 s14, v254, 4
	v_readlane_b32 s15, v254, 5
	s_waitcnt lgkmcnt(0)
	s_mov_b64 s[36:37], s[14:15]
	s_mov_b32 s0, s2
	v_readlane_b32 s13, v254, 3
	s_mov_b64 s[0:1], s[12:13]
	v_mov_b32_e32 v178, v0
	v_readfirstlane_b32 s101, v0
	s_nop 3
	s_and_b32 s101, s101, 0x3ff
	s_lshr_b32 s101, s101, 6
	s_cmp_ge_u32 s101, 4
	s_cbranch_scc1 .Lattn_prio_done
	s_setprio 1
